# speedup vs baseline: 1.0044x; 1.0008x over previous
_Z15gemm_out_kernelPKDF16_S0_Pf:
	s_load_dwordx4 s[16:19], s[0:1], 0x0
	s_load_dwordx2 s[4:5], s[0:1], 0x10
	s_lshl_b32 s0, s2, 2
	s_and_b32 s0, s0, 28
	s_bfe_u32 s1, s2, 0x20003
	s_lshr_b32 s8, s2, 5
	v_readfirstlane_b32 s10, v0
	s_or_b32 s9, s0, s1
	s_lshr_b32 s13, s10, 6
	s_mov_b32 s1, 0
	s_lshl_b32 s0, s8, 1
	s_lshr_b32 s14, s10, 8
	s_lshl_b32 s2, s9, 19
	s_lshl_b64 s[6:7], s[0:1], 19
	s_lshl_b32 s0, s13, 10
	s_waitcnt lgkmcnt(0)
	s_add_u32 s2, s16, s2
	s_addc_u32 s3, s17, 0
	s_add_i32 s0, s0, 0
	v_lshlrev_b32_e32 v64, 4, v0
	s_mov_b32 m0, s0
	v_or_b32_e32 v66, 0x2000, v64
	global_load_lds_dwordx4 v64, s[2:3]
	s_add_i32 m0, s0, 0x2000
	v_mov_b32_e32 v67, 0
	s_add_u32 s6, s18, s6
	v_mov_b32_e32 v65, v67
	global_load_lds_dwordx4 v66, s[2:3]
	s_addc_u32 s7, s19, s7
	s_add_i32 m0, s0, 0x4000
	v_lshl_add_u64 v[68:69], s[6:7], 0, v[64:65]
	global_load_lds_dwordx4 v64, s[6:7]
	s_mov_b64 s[6:7], 0x2000
	v_lshl_add_u64 v[2:3], v[68:69], 0, s[6:7]
	s_add_i32 m0, s0, 0x6000
	s_mov_b64 s[16:17], 0x80000
	global_load_lds_dwordx4 v[2:3], off
	s_add_i32 m0, s0, 0x8000
	v_lshl_add_u64 v[70:71], v[68:69], 0, s[16:17]
	global_load_lds_dwordx4 v[70:71], off
	s_mov_b64 s[16:17], 0x82000
	s_add_i32 m0, s0, 0xa000
	v_lshl_add_u64 v[72:73], v[68:69], 0, s[16:17]
	s_add_u32 s18, s2, 0x4000
	global_load_lds_dwordx4 v[72:73], off
	s_addc_u32 s19, s3, 0
	s_add_i32 m0, s0, 0xc000
	s_mov_b64 s[16:17], 0x4000
	global_load_lds_dwordx4 v64, s[18:19]
	s_add_i32 m0, s0, 0xe000
	v_lshl_add_u64 v[2:3], v[68:69], 0, s[16:17]
	global_load_lds_dwordx4 v66, s[18:19]
	s_add_i32 m0, s0, 0x10000
	s_mov_b64 s[16:17], 0x6000
	global_load_lds_dwordx4 v[2:3], off
	v_lshl_add_u64 v[2:3], v[68:69], 0, s[16:17]
	s_add_i32 m0, s0, 0x12000
	s_mov_b64 s[16:17], 0x84000
	global_load_lds_dwordx4 v[2:3], off
	s_add_i32 m0, s0, 0x14000
	v_lshl_add_u64 v[2:3], v[68:69], 0, s[16:17]
	s_mov_b64 s[16:17], 0x86000
	global_load_lds_dwordx4 v[2:3], off
	v_lshl_add_u64 v[2:3], v[68:69], 0, s[16:17]
	s_add_i32 m0, s0, 0x16000
	s_mov_b32 s12, 2
	global_load_lds_dwordx4 v[2:3], off
	s_waitcnt vmcnt(6)
	s_cmpk_lt_u32 s10, 0x100
	s_barrier
	s_cbranch_scc1 .LBB2_2
	s_barrier
.LBB2_2:
	v_lshrrev_b32_e32 v1, 1, v0
	v_and_b32_e32 v75, 24, v1
	s_lshl_b32 s13, s13, 5
	v_and_b32_e32 v74, 15, v0
	v_lshlrev_b32_e32 v1, 1, v75
	v_lshlrev_b32_e32 v2, 6, v0
	s_movk_i32 s15, 0x3c0
	v_lshlrev_b32_e32 v0, 2, v0
	s_and_b32 s13, s13, 0x60
	s_lshl_b32 s11, s14, 6
	v_and_or_b32 v2, v2, s15, v1
	v_and_b32_e32 v0, 32, v0
	s_lshl_b32 s15, s13, 7
	s_lshl_b32 s14, s14, 13
	v_lshl_or_b32 v1, v74, 6, v1
	v_bitop3_b32 v2, s15, v2, v0 bitop3:0xf6
	s_add_i32 s14, s14, 0
	v_xad_u32 v76, v1, v0, s14
	v_add_u32_e32 v77, 0, v2
	s_mov_b32 s14, 0
	v_mov_b32_e32 v8, v67
	v_mov_b32_e32 v9, v67
	v_mov_b32_e32 v10, v67
	v_mov_b32_e32 v11, v67
	v_mov_b32_e32 v24, v67
	v_mov_b32_e32 v25, v67
	v_mov_b32_e32 v26, v67
	v_mov_b32_e32 v27, v67
	v_mov_b32_e32 v12, v67
	v_mov_b32_e32 v13, v67
	v_mov_b32_e32 v14, v67
	v_mov_b32_e32 v15, v67
	v_mov_b32_e32 v28, v67
	v_mov_b32_e32 v29, v67
	v_mov_b32_e32 v30, v67
	v_mov_b32_e32 v31, v67
	v_mov_b32_e32 v0, v67
	v_mov_b32_e32 v1, v67
	v_mov_b32_e32 v2, v67
	v_mov_b32_e32 v3, v67
	v_mov_b32_e32 v16, v67
	v_mov_b32_e32 v17, v67
	v_mov_b32_e32 v18, v67
	v_mov_b32_e32 v19, v67
	v_mov_b32_e32 v4, v67
	v_mov_b32_e32 v5, v67
	v_mov_b32_e32 v6, v67
	v_mov_b32_e32 v7, v67
	v_mov_b32_e32 v20, v67
	v_mov_b32_e32 v21, v67
	v_mov_b32_e32 v22, v67
	v_mov_b32_e32 v23, v67
	v_mov_b32_e32 v40, v67
	v_mov_b32_e32 v41, v67
	v_mov_b32_e32 v42, v67
	v_mov_b32_e32 v43, v67
	v_mov_b32_e32 v56, v67
	v_mov_b32_e32 v57, v67
	v_mov_b32_e32 v58, v67
	v_mov_b32_e32 v59, v67
	v_mov_b32_e32 v48, v67
	v_mov_b32_e32 v49, v67
	v_mov_b32_e32 v50, v67
	v_mov_b32_e32 v51, v67
	v_mov_b32_e32 v60, v67
	v_mov_b32_e32 v61, v67
	v_mov_b32_e32 v62, v67
	v_mov_b32_e32 v63, v67
	v_mov_b32_e32 v36, v67
	v_mov_b32_e32 v37, v67
	v_mov_b32_e32 v38, v67
	v_mov_b32_e32 v39, v67
	v_mov_b32_e32 v52, v67
	v_mov_b32_e32 v53, v67
	v_mov_b32_e32 v54, v67
	v_mov_b32_e32 v55, v67
	v_mov_b32_e32 v32, v67
	v_mov_b32_e32 v33, v67
	v_mov_b32_e32 v34, v67
	v_mov_b32_e32 v35, v67
	v_mov_b32_e32 v44, v67
	v_mov_b32_e32 v45, v67
	v_mov_b32_e32 v46, v67
	v_mov_b32_e32 v47, v67
	s_cmpk_lt_u32 s10, 0x100
	s_cbranch_scc1 .Lout_noprio
	s_setprio 1
.Lout_noprio:
.LBB2_3:
	s_cmp_lt_u32 s14, 30
	s_cselect_b32 s16, 2, 0xffffffe2
	s_add_i32 s16, s16, s14
	s_ashr_i32 s17, s16, 31
	s_mul_i32 s15, s1, 0xc000
	s_lshl_b64 s[16:17], s[16:17], 14
	v_add_u32_e32 v106, s15, v77
	v_add_u32_e32 v138, s15, v76
	s_mul_i32 s15, s12, 0xc000
	s_add_u32 s18, s2, s16
	s_addc_u32 s19, s3, s17
	s_add_i32 s15, s0, s15
	v_lshl_add_u64 v[142:143], s[18:19], 0, v[64:65]
	s_mov_b32 m0, s15
	ds_read_b128 v[78:81], v106 offset:16384
	ds_read_b128 v[82:85], v106 offset:17408
	ds_read_b128 v[86:89], v106 offset:32768
	ds_read_b128 v[90:93], v106 offset:33792
	ds_read_b128 v[94:97], v106 offset:18432
	ds_read_b128 v[98:101], v106 offset:19456
	ds_read_b128 v[102:105], v106 offset:34816
	ds_read_b128 v[106:109], v106 offset:35840
	ds_read_b128 v[110:113], v138
	ds_read_b128 v[114:117], v138 offset:1024
	ds_read_b128 v[118:121], v138 offset:2048
	ds_read_b128 v[122:125], v138 offset:3072
	ds_read_b128 v[126:129], v138 offset:4096
	ds_read_b128 v[130:133], v138 offset:5120
	ds_read_b128 v[134:137], v138 offset:6144
	ds_read_b128 v[138:141], v138 offset:7168
	global_load_lds_dwordx4 v[142:143], off
	v_lshl_add_u64 v[142:143], s[18:19], 0, v[66:67]
	s_add_i32 m0, s15, 0x2000
	s_nop 0
	global_load_lds_dwordx4 v[142:143], off
	v_lshl_add_u64 v[142:143], v[68:69], 0, s[16:17]
	s_add_i32 m0, s15, 0x4000
	s_nop 0
	global_load_lds_dwordx4 v[142:143], off
	s_waitcnt vmcnt(3) lgkmcnt(0)
	s_barrier
	s_nop 0
	v_mfma_f32_16x16x32_f16 v[8:11], v[78:81], v[110:113], v[8:11]
	v_lshl_add_u64 v[144:145], v[72:73], 0, s[16:17]
	s_add_i32 s18, s15, 0xa000
	v_lshl_add_u64 v[146:147], v[70:71], 0, s[16:17]
	v_mfma_f32_16x16x32_f16 v[24:27], v[94:97], v[110:113], v[24:27]
	s_add_i32 s16, s15, 0x8000
	v_lshl_add_u64 v[142:143], v[142:143], 0, s[6:7]
	s_add_i32 m0, s15, 0x6000
	v_mfma_f32_16x16x32_f16 v[8:11], v[82:85], v[114:117], v[8:11]
	v_mfma_f32_16x16x32_f16 v[24:27], v[98:101], v[114:117], v[24:27]
	global_load_lds_dwordx4 v[142:143], off
	v_mfma_f32_16x16x32_f16 v[12:15], v[78:81], v[118:121], v[12:15]
	v_mfma_f32_16x16x32_f16 v[28:31], v[94:97], v[118:121], v[28:31]
	v_mfma_f32_16x16x32_f16 v[12:15], v[82:85], v[122:125], v[12:15]
	v_mfma_f32_16x16x32_f16 v[28:31], v[98:101], v[122:125], v[28:31]
	v_mfma_f32_16x16x32_f16 v[0:3], v[78:81], v[126:129], v[0:3]
	v_mfma_f32_16x16x32_f16 v[16:19], v[94:97], v[126:129], v[16:19]
	v_mfma_f32_16x16x32_f16 v[0:3], v[82:85], v[130:133], v[0:3]
	v_mfma_f32_16x16x32_f16 v[16:19], v[98:101], v[130:133], v[16:19]
	s_mov_b32 m0, s16
	v_mfma_f32_16x16x32_f16 v[4:7], v[78:81], v[134:137], v[4:7]
	global_load_lds_dwordx4 v[146:147], off
	v_mfma_f32_16x16x32_f16 v[20:23], v[94:97], v[134:137], v[20:23]
	v_mfma_f32_16x16x32_f16 v[4:7], v[82:85], v[138:141], v[4:7]
	v_mfma_f32_16x16x32_f16 v[20:23], v[98:101], v[138:141], v[20:23]
	v_mfma_f32_16x16x32_f16 v[40:43], v[86:89], v[110:113], v[40:43]
	v_mfma_f32_16x16x32_f16 v[56:59], v[102:105], v[110:113], v[56:59]
	v_mfma_f32_16x16x32_f16 v[40:43], v[90:93], v[114:117], v[40:43]
	v_mfma_f32_16x16x32_f16 v[56:59], v[106:109], v[114:117], v[56:59]
	s_mov_b32 m0, s18
	v_mfma_f32_16x16x32_f16 v[48:51], v[86:89], v[118:121], v[48:51]
	global_load_lds_dwordx4 v[144:145], off
	v_mfma_f32_16x16x32_f16 v[60:63], v[102:105], v[118:121], v[60:63]
	v_mfma_f32_16x16x32_f16 v[48:51], v[90:93], v[122:125], v[48:51]
	v_mfma_f32_16x16x32_f16 v[60:63], v[106:109], v[122:125], v[60:63]
	v_mfma_f32_16x16x32_f16 v[36:39], v[86:89], v[126:129], v[36:39]
	v_mfma_f32_16x16x32_f16 v[52:55], v[102:105], v[126:129], v[52:55]
	v_mfma_f32_16x16x32_f16 v[36:39], v[90:93], v[130:133], v[36:39]
	v_mfma_f32_16x16x32_f16 v[52:55], v[106:109], v[130:133], v[52:55]
	v_mfma_f32_16x16x32_f16 v[32:35], v[86:89], v[134:137], v[32:35]
	v_mfma_f32_16x16x32_f16 v[44:47], v[102:105], v[134:137], v[44:47]
	v_mfma_f32_16x16x32_f16 v[32:35], v[90:93], v[138:141], v[32:35]
	v_mfma_f32_16x16x32_f16 v[44:47], v[106:109], v[138:141], v[44:47]
	s_nop 0
	s_barrier
	s_add_i32 s15, s1, 1
	s_cmp_lg_u32 s1, 2
	s_cselect_b32 s1, s15, 0
	s_add_i32 s15, s12, 1
	s_cmp_lg_u32 s12, 2
	s_cselect_b32 s12, s15, 0
	s_add_i32 s14, s14, 1
	s_cmp_eq_u32 s14, 32
	s_cbranch_scc0 .LBB2_3
	s_cmpk_lt_u32 s10, 0x100
	s_cbranch_scc0 .LBB2_6
	s_barrier
